# baseline (speedup 1.0000x reference)
.LBB0_118:
	s_or_b64 exec, exec, s[60:61]
	s_setprio 0
	v_readfirstlane_b32 s74, v0
	v_mov_b32_e32 v36, 0x26d50
	ds_read_b128 v[42:45], v36
	s_lshr_b32 s74, s74, 6
	s_and_b32 s74, s74, 3
	s_waitcnt lgkmcnt(0)
	v_readfirstlane_b32 s94, v42
	v_readfirstlane_b32 s95, v43
	v_readfirstlane_b32 s96, v44
	v_readfirstlane_b32 s97, v45
	s_lshl_b32 s94, s94, 2
	s_lshl_b32 s95, s95, 2
	s_lshl_b32 s96, s96, 2
	s_lshl_b32 s97, s97, 2
	s_sub_i32 s98, 0, s74
	s_and_b32 s98, s98, 3
	s_or_b32 s94, s94, s98
	s_sub_i32 s98, 1, s74
	s_and_b32 s98, s98, 3
	s_or_b32 s95, s95, s98
	s_sub_i32 s98, 2, s74
	s_and_b32 s98, s98, 3
	s_or_b32 s96, s96, s98
	s_sub_i32 s98, 3, s74
	s_and_b32 s98, s98, 3
	s_or_b32 s97, s97, s98
	s_min_u32 s94, s94, s95
	s_min_u32 s96, s96, s97
	s_min_u32 s94, s94, s96
	s_and_b32 s94, s94, 3
	s_add_i32 s74, s74, s94
	s_and_b32 s74, s74, 3
	v_mov_b32_e32 v42, 0
	v_mov_b32_e32 v50, 0
	v_mov_b32_e32 v36, s74
	v_lshl_or_b32 v44, v36, 13, v86
	v_mov_b32_e32 v45, 0
	v_lshl_add_u64 v[18:19], s[56:57], 0, v[44:45]
	v_add_co_u32_e32 v34, vcc, 0x1000, v18
	global_load_dwordx4 v[2:5], v44, s[56:57]
	global_load_dwordx4 v[6:9], v44, s[56:57] offset:1024
	global_load_dwordx4 v[10:13], v44, s[56:57] offset:2048
	global_load_dwordx4 v[14:17], v44, s[56:57] offset:3072
	v_addc_co_u32_e32 v35, vcc, 0, v19, vcc
	v_lshlrev_b32_e32 v44, 7, v36
	global_load_dwordx4 v[18:21], v[34:35], off
	global_load_dwordx4 v[22:25], v[34:35], off offset:1024
	global_load_dwordx4 v[26:29], v[34:35], off offset:2048
	global_load_dwordx4 v[30:33], v[34:35], off offset:3072
	v_lshl_add_u64 v[34:35], s[52:53], 0, v[44:45]
	v_lshlrev_b32_e32 v36, 2, v1
	v_mov_b32_e32 v37, v45
	v_lshl_add_u64 v[46:47], v[34:35], 0, v[36:37]
	global_load_dwordx4 v[34:37], v[46:47], off offset:16
	global_load_dwordx4 v[38:41], v[46:47], off
	v_add3_u32 v46, s66, v50, v79
	v_ashrrev_i32_e32 v47, 31, v46
	v_and_b32_e32 v0, 48, v0
	v_lshlrev_b64 v[46:47], 9, v[46:47]
	v_lshlrev_b32_e32 v0, 1, v0
	v_or3_b32 v46, v46, v44, v0
	v_mul_u32_u24_e32 v43, 0x110, v79
	s_movk_i32 s0, 0x1100
	v_lshl_add_u64 v[0:1], s[54:55], 0, v[46:47]
	v_mad_u32_u24 v42, v42, s0, v43
	s_mov_b32 s0, 0x10000
	v_lshl_add_u64 v[0:1], v[0:1], 0, 16
	v_add3_u32 v51, v42, v70, s0
	s_lshl_b32 s75, s74, 2
	s_add_i32 s75, s75, 0x26d50
	s_add_i32 s76, s33, 15
	s_lshr_b32 s76, s76, 4
	v_mov_b64_e32 v[60:61], v[0:1]
	v_mov_b32_e32 v62, v51
	s_mov_b32 s96, 1
